# speedup vs baseline: 1.0215x; 1.0072x over previous
_Z6gat_k1PKfS0_S0_S0_PDF16_S1_S1_Pf:
	s_load_dwordx8 s[4:11], s[0:1], 0x0
	s_load_dwordx8 s[12:19], s[0:1], 0x20
	v_lshrrev_b32_e32 v54, 6, v0
	v_and_b32_e32 v57, 0xc0, v0
	s_lshl_b32 s3, s2, 5
	v_and_b32_e32 v1, 63, v0
	v_bfe_u32 v55, v0, 5, 1
	v_lshlrev_b32_e32 v2, 8, v57
	v_mov_b32_e32 v19, 0
	v_or_b32_e32 v4, s3, v54
	v_and_b32_e32 v56, 31, v0
	v_lshl_or_b32 v18, v55, 11, v2
	v_lshlrev_b32_e32 v20, 4, v1
	v_mov_b32_e32 v21, v19
	v_ashrrev_i32_e32 v5, 31, v4
	s_waitcnt lgkmcnt(0)
	v_lshl_add_u64 v[2:3], s[6:7], 0, v[18:19]
	v_lshlrev_b32_e32 v18, 2, v56
	v_lshl_add_u64 v[6:7], s[4:5], 0, v[20:21]
	v_lshlrev_b64 v[8:9], 10, v[4:5]
	v_lshl_add_u64 v[2:3], v[2:3], 0, v[18:19]
	v_lshl_add_u64 v[10:11], v[6:7], 0, v[8:9]
	v_or_b32_e32 v12, 0x1000, v8
	v_mov_b32_e32 v13, v9
	global_load_dword v58, v[2:3], off
	global_load_dword v59, v[2:3], off offset:128
	global_load_dword v60, v[2:3], off offset:256
	global_load_dword v61, v[2:3], off offset:384
	global_load_dword v62, v[2:3], off offset:512
	global_load_dword v63, v[2:3], off offset:640
	global_load_dword v64, v[2:3], off offset:768
	global_load_dword v65, v[2:3], off offset:896
	v_lshl_add_u64 v[12:13], v[6:7], 0, v[12:13]
	global_load_dwordx4 v[22:25], v[10:11], off nt
	global_load_dwordx4 v[26:29], v[12:13], off nt
	v_or_b32_e32 v10, 0x2000, v8
	v_mov_b32_e32 v11, v9
	v_or_b32_e32 v8, 0x3000, v8
	v_lshl_add_u64 v[10:11], v[6:7], 0, v[10:11]
	v_lshl_add_u64 v[8:9], v[6:7], 0, v[8:9]
	global_load_dwordx4 v[30:33], v[10:11], off nt
	global_load_dwordx4 v[34:37], v[8:9], off nt
	v_or_b32_e32 v8, 16, v4
	v_ashrrev_i32_e32 v9, 31, v8
	v_or_b32_e32 v10, 20, v4
	v_lshlrev_b64 v[8:9], 10, v[8:9]
	v_ashrrev_i32_e32 v11, 31, v10
	v_lshl_add_u64 v[8:9], v[6:7], 0, v[8:9]
	v_lshlrev_b64 v[10:11], 10, v[10:11]
	v_lshl_add_u64 v[10:11], v[6:7], 0, v[10:11]
	global_load_dwordx4 v[38:41], v[8:9], off nt
	global_load_dwordx4 v[42:45], v[10:11], off nt
	v_or_b32_e32 v8, 24, v4
	v_ashrrev_i32_e32 v9, 31, v8
	v_or_b32_e32 v4, 28, v4
	v_lshlrev_b64 v[8:9], 10, v[8:9]
	v_ashrrev_i32_e32 v5, 31, v4
	v_lshl_add_u64 v[8:9], v[6:7], 0, v[8:9]
	v_lshlrev_b64 v[4:5], 10, v[4:5]
	v_lshl_add_u64 v[4:5], v[6:7], 0, v[4:5]
	global_load_dwordx4 v[46:49], v[8:9], off nt
	global_load_dwordx4 v[50:53], v[4:5], off nt
	global_load_dword v19, v[2:3], off offset:1024
	global_load_dword v66, v[2:3], off offset:1152
	global_load_dword v67, v[2:3], off offset:1280
	global_load_dword v68, v[2:3], off offset:1408
	global_load_dword v69, v[2:3], off offset:1536
	global_load_dword v70, v[2:3], off offset:1664
	global_load_dword v71, v[2:3], off offset:1792
	global_load_dword v72, v[2:3], off offset:1920
	s_movk_i32 s4, 0x1000
	v_add_co_u32_e32 v4, vcc, s4, v2
	s_movk_i32 s4, 0x2000
	s_nop 0
	v_addc_co_u32_e32 v5, vcc, 0, v3, vcc
	v_add_co_u32_e32 v6, vcc, s4, v2
	s_movk_i32 s4, 0x3000
	s_nop 0
	v_addc_co_u32_e32 v7, vcc, 0, v3, vcc
	global_load_dword v73, v[4:5], off offset:128
	global_load_dword v74, v[4:5], off offset:256
	global_load_dword v75, v[4:5], off offset:384
	global_load_dword v76, v[4:5], off offset:512
	global_load_dword v77, v[4:5], off offset:640
	global_load_dword v78, v[4:5], off offset:768
	global_load_dword v79, v[4:5], off offset:896
	global_load_dword v80, v[4:5], off offset:1024
	global_load_dword v81, v[4:5], off offset:1152
	global_load_dword v82, v[4:5], off offset:1280
	global_load_dword v83, v[4:5], off offset:1408
	global_load_dword v84, v[4:5], off offset:1536
	global_load_dword v85, v[4:5], off offset:1664
	global_load_dword v86, v[4:5], off offset:1792
	global_load_dword v87, v[4:5], off offset:1920
	global_load_dword v88, v[6:7], off offset:-4096
	global_load_dword v89, v[6:7], off
	global_load_dword v90, v[6:7], off offset:128
	global_load_dword v91, v[6:7], off offset:256
	global_load_dword v92, v[6:7], off offset:384
	global_load_dword v93, v[6:7], off offset:512
	global_load_dword v94, v[6:7], off offset:640
	global_load_dword v95, v[6:7], off offset:768
	global_load_dword v96, v[6:7], off offset:896
	global_load_dword v97, v[6:7], off offset:1024
	global_load_dword v98, v[6:7], off offset:1152
	global_load_dword v99, v[6:7], off offset:1280
	global_load_dword v100, v[6:7], off offset:1408
	global_load_dword v101, v[6:7], off offset:1536
	global_load_dword v102, v[6:7], off offset:1664
	global_load_dword v103, v[6:7], off offset:1792
	global_load_dword v104, v[6:7], off offset:1920
	v_add_co_u32_e32 v2, vcc, s4, v2
	v_and_b32_e32 v1, 7, v0
	s_nop 0
	v_addc_co_u32_e32 v3, vcc, 0, v3, vcc
	global_load_dword v105, v[2:3], off
	global_load_dword v106, v[2:3], off offset:128
	global_load_dword v107, v[2:3], off offset:256
	global_load_dword v108, v[2:3], off offset:384
	global_load_dword v109, v[2:3], off offset:512
	global_load_dword v110, v[2:3], off offset:640
	global_load_dword v111, v[2:3], off offset:768
	global_load_dword v112, v[2:3], off offset:896
	global_load_dword v113, v[2:3], off offset:1024
	global_load_dword v114, v[2:3], off offset:1152
	global_load_dword v115, v[2:3], off offset:1280
	global_load_dword v116, v[2:3], off offset:1408
	global_load_dword v117, v[2:3], off offset:1536
	global_load_dword v118, v[2:3], off offset:1664
	global_load_dword v119, v[2:3], off offset:1792
	global_load_dword v120, v[2:3], off offset:1920
	v_lshlrev_b32_e32 v121, 5, v1
	global_load_dwordx4 v[6:9], v121, s[8:9]
	global_load_dwordx4 v[2:5], v121, s[10:11]
	global_load_dwordx4 v[14:17], v121, s[8:9] offset:16
	global_load_dwordx4 v[10:13], v121, s[10:11] offset:16
	s_movk_i32 s4, 0x410
	v_mad_u32_u24 v122, v54, s4, v20
	s_movk_i32 s8, 0x110
	s_waitcnt vmcnt(62)
	ds_write_b128 v122, v[22:25] offset:34816
	ds_write_b128 v122, v[26:29] offset:38976
	ds_write_b128 v122, v[30:33] offset:43136
	ds_write_b128 v122, v[34:37] offset:47296
	ds_write_b128 v122, v[38:41] offset:51456
	ds_write_b128 v122, v[42:45] offset:55616
	s_waitcnt vmcnt(61)
	ds_write_b128 v122, v[46:49] offset:59776
	s_waitcnt vmcnt(60)
	ds_write_b128 v122, v[50:53] offset:63936
	v_mul_u32_u24_e32 v22, 0x410, v56
	v_lshlrev_b32_e32 v23, 2, v57
	v_and_b32_e32 v24, 32, v0
	v_add3_u32 v38, v22, v23, v24
	s_waitcnt lgkmcnt(0)
	s_barrier
	ds_read_b128 v[22:25], v38 offset:34832
	ds_read_b128 v[26:29], v38 offset:34816
	ds_read_b128 v[30:33], v38 offset:34880
	ds_read_b128 v[34:37], v38 offset:34896
	s_waitcnt lgkmcnt(3)
	v_cvt_pk_f16_f32 v25, v24, v25
	v_cvt_pk_f16_f32 v24, v22, v23
	s_waitcnt lgkmcnt(2)
	v_cvt_pk_f16_f32 v23, v28, v29
	v_cvt_pk_f16_f32 v22, v26, v27
	s_waitcnt vmcnt(53)
	v_cvt_pk_f16_f32 v29, v69, v71
	v_cvt_pk_f16_f32 v28, v19, v67
	v_cvt_pk_f16_f32 v27, v62, v64
	v_cvt_pk_f16_f32 v26, v58, v60
	v_lshlrev_b32_e32 v19, 2, v55
	s_nop 0
	v_mfma_f32_32x32x16_f16 a[0:15], v[22:25], v[26:29], 0
	s_waitcnt vmcnt(52)
	v_cvt_pk_f16_f32 v29, v70, v72
	v_cvt_pk_f16_f32 v28, v66, v68
	v_cvt_pk_f16_f32 v27, v63, v65
	v_cvt_pk_f16_f32 v26, v59, v61
	s_nop 1
	v_mfma_f32_32x32x16_f16 a[16:31], v[22:25], v[26:29], 0
	s_waitcnt lgkmcnt(0)
	v_cvt_pk_f16_f32 v25, v36, v37
	v_cvt_pk_f16_f32 v24, v34, v35
	v_cvt_pk_f16_f32 v23, v32, v33
	v_cvt_pk_f16_f32 v22, v30, v31
	ds_read_b128 v[30:33], v38 offset:34944
	ds_read_b128 v[34:37], v38 offset:34960
	s_waitcnt vmcnt(38)
	v_cvt_pk_f16_f32 v29, v84, v86
	v_cvt_pk_f16_f32 v28, v80, v82
	v_cvt_pk_f16_f32 v27, v76, v78
	s_waitcnt vmcnt(36)
	v_cvt_pk_f16_f32 v26, v88, v74
	s_nop 1
	v_mfma_f32_32x32x16_f16 a[0:15], v[22:25], v[26:29], a[0:15]
	v_cvt_pk_f16_f32 v29, v85, v87
	v_cvt_pk_f16_f32 v28, v81, v83
	v_cvt_pk_f16_f32 v27, v77, v79
	v_cvt_pk_f16_f32 v26, v73, v75
	s_nop 1
	v_mfma_f32_32x32x16_f16 a[16:31], v[22:25], v[26:29], a[16:31]
	s_waitcnt lgkmcnt(0)
	v_cvt_pk_f16_f32 v25, v36, v37
	v_cvt_pk_f16_f32 v24, v34, v35
	v_cvt_pk_f16_f32 v23, v32, v33
	v_cvt_pk_f16_f32 v22, v30, v31
	ds_read_b128 v[30:33], v38 offset:35008
	ds_read_b128 v[34:37], v38 offset:35024
	s_waitcnt vmcnt(21)
	v_cvt_pk_f16_f32 v29, v101, v103
	v_cvt_pk_f16_f32 v28, v97, v99
	v_cvt_pk_f16_f32 v27, v93, v95
	v_cvt_pk_f16_f32 v26, v89, v91
	s_nop 1
	v_mfma_f32_32x32x16_f16 a[0:15], v[22:25], v[26:29], a[0:15]
	s_waitcnt vmcnt(20)
	v_cvt_pk_f16_f32 v29, v102, v104
	v_cvt_pk_f16_f32 v28, v98, v100
	v_cvt_pk_f16_f32 v27, v94, v96
	v_cvt_pk_f16_f32 v26, v90, v92
	s_nop 1
	v_mfma_f32_32x32x16_f16 a[16:31], v[22:25], v[26:29], a[16:31]
	s_waitcnt lgkmcnt(0)
	v_cvt_pk_f16_f32 v25, v36, v37
	v_cvt_pk_f16_f32 v24, v34, v35
	v_cvt_pk_f16_f32 v23, v32, v33
	v_cvt_pk_f16_f32 v22, v30, v31
	s_waitcnt vmcnt(5)
	v_cvt_pk_f16_f32 v29, v117, v119
	v_cvt_pk_f16_f32 v28, v113, v115
	v_cvt_pk_f16_f32 v27, v109, v111
	v_cvt_pk_f16_f32 v26, v105, v107
	s_nop 1
	v_mfma_f32_32x32x16_f16 a[0:15], v[22:25], v[26:29], a[0:15]
	s_waitcnt vmcnt(4)
	v_cvt_pk_f16_f32 v29, v118, v120
	v_cvt_pk_f16_f32 v28, v114, v116
	v_cvt_pk_f16_f32 v27, v110, v112
	v_cvt_pk_f16_f32 v26, v106, v108
	s_nop 1
	v_mfma_f32_32x32x16_f16 a[16:31], v[22:25], v[26:29], a[16:31]
	v_lshl_or_b32 v22, v54, 5, v19
	v_mul_u32_u24_e32 v22, 0x44, v22
	v_lshl_add_u32 v22, v22, 2, v18
	s_nop 0
	ds_write_b32 v22, a0
	s_nop 6
	ds_write_b32 v22, a16 offset:128
	ds_write_b32 v22, a1 offset:272
	ds_write_b32 v22, a17 offset:400
	ds_write_b32 v22, a2 offset:544
	ds_write_b32 v22, a18 offset:672
	ds_write_b32 v22, a3 offset:816
	ds_write_b32 v22, a19 offset:944
	ds_write_b32 v22, a4 offset:2176
	ds_write_b32 v22, a20 offset:2304
	ds_write_b32 v22, a5 offset:2448
	ds_write_b32 v22, a21 offset:2576
	ds_write_b32 v22, a6 offset:2720
	ds_write_b32 v22, a22 offset:2848
	ds_write_b32 v22, a7 offset:2992
	ds_write_b32 v22, a23 offset:3120
	ds_write_b32 v22, a8 offset:4352
	ds_write_b32 v22, a24 offset:4480
	ds_write_b32 v22, a9 offset:4624
	ds_write_b32 v22, a25 offset:4752
	ds_write_b32 v22, a10 offset:4896
	ds_write_b32 v22, a26 offset:5024
	ds_write_b32 v22, a11 offset:5168
	ds_write_b32 v22, a27 offset:5296
	ds_write_b32 v22, a12 offset:6528
	ds_write_b32 v22, a28 offset:6656
	ds_write_b32 v22, a13 offset:6800
	ds_write_b32 v22, a29 offset:6928
	ds_write_b32 v22, a14 offset:7072
	ds_write_b32 v22, a30 offset:7200
	ds_write_b32 v22, a15 offset:7344
	ds_write_b32 v22, a31 offset:7472
	v_lshrrev_b32_e32 v22, 3, v0
	v_mad_u32_u24 v23, v22, s8, v121
	s_waitcnt lgkmcnt(0)
	s_barrier
	ds_read_b128 v[24:27], v23
	ds_read_b128 v[28:31], v23 offset:16
	ds_read_b128 v[32:35], v23 offset:8704
	s_waitcnt lgkmcnt(2)
	v_pk_add_f32 v[36:37], v[26:27], 0 op_sel_hi:[1,0]
	v_pk_add_f32 v[38:39], v[24:25], 0 op_sel_hi:[1,0]
	ds_read_b128 v[24:27], v23 offset:8720
	s_waitcnt lgkmcnt(2)
	v_pk_add_f32 v[40:41], v[30:31], 0 op_sel_hi:[1,0]
	v_pk_add_f32 v[42:43], v[28:29], 0 op_sel_hi:[1,0]
	ds_read_b128 v[28:31], v23 offset:17408
	s_waitcnt lgkmcnt(2)
	v_pk_add_f32 v[34:35], v[36:37], v[34:35]
	v_pk_add_f32 v[36:37], v[38:39], v[32:33]
	s_waitcnt lgkmcnt(1)
	v_pk_add_f32 v[38:39], v[40:41], v[26:27]
	v_pk_add_f32 v[40:41], v[42:43], v[24:25]
	ds_read_b128 v[24:27], v23 offset:17424
	s_waitcnt lgkmcnt(1)
	v_pk_add_f32 v[42:43], v[34:35], v[30:31]
	ds_read_b128 v[30:33], v23 offset:26112
	v_pk_add_f32 v[28:29], v[36:37], v[28:29]
	ds_read_b128 v[34:37], v23 offset:26128
	s_waitcnt lgkmcnt(2)
	v_pk_add_f32 v[40:41], v[40:41], v[24:25]
	v_pk_add_f32 v[38:39], v[38:39], v[26:27]
	s_waitcnt lgkmcnt(1)
	v_pk_add_f32 v[24:25], v[28:29], v[30:31]
	v_pk_add_f32 v[26:27], v[42:43], v[32:33]
	s_waitcnt lgkmcnt(0)
	v_pk_add_f32 v[28:29], v[40:41], v[34:35]
	v_pk_add_f32 v[30:31], v[38:39], v[36:37]
	s_waitcnt vmcnt(0)
	v_mul_f32_e32 v10, v28, v10
	v_fmac_f32_e32 v10, v24, v2
	v_mul_f32_e32 v14, v28, v14
	v_add_f32_e32 v2, 0, v10
	v_mul_f32_e32 v10, v29, v15
	v_fmac_f32_e32 v14, v24, v6
	v_fmac_f32_e32 v10, v25, v7
	v_mul_f32_e32 v7, v29, v11
	v_add_f32_e32 v6, 0, v14
	v_fmac_f32_e32 v7, v25, v3
	v_mul_f32_e32 v3, v30, v16
	v_add_f32_e32 v6, v6, v10
	v_fmac_f32_e32 v3, v26, v8
	v_add_f32_e32 v3, v6, v3
	v_mul_f32_e32 v6, v30, v12
	v_fmac_f32_e32 v6, v26, v4
	v_mul_f32_e32 v4, v31, v17
	v_fmac_f32_e32 v4, v27, v9
	v_add_f32_e32 v2, v2, v7
	v_add_f32_e32 v3, v3, v4
	v_mul_f32_e32 v4, v31, v13
	v_add_f32_e32 v2, v2, v6
	v_fmac_f32_e32 v4, v27, v5
	v_add_f32_e32 v2, v2, v4
	ds_write_b128 v23, v[24:27]
	ds_write_b128 v23, v[28:31] offset:16
	s_nop 1
	v_add_f32_dpp v3, v3, v3 quad_perm:[1,0,3,2] row_mask:0xf bank_mask:0xf
	v_add_f32_dpp v6, v2, v2 quad_perm:[1,0,3,2] row_mask:0xf bank_mask:0xf
	s_nop 1
	v_add_f32_dpp v3, v3, v3 quad_perm:[2,3,0,1] row_mask:0xf bank_mask:0xf
	v_add_f32_dpp v6, v6, v6 quad_perm:[2,3,0,1] row_mask:0xf bank_mask:0xf
	s_nop 1
	v_add_f32_dpp v2, v3, v3 row_half_mirror row_mask:0xf bank_mask:0xf
	v_add_f32_dpp v3, v6, v6 row_half_mirror row_mask:0xf bank_mask:0xf
	v_cmp_eq_u32_e32 vcc, 0, v1
	s_and_saveexec_b64 s[6:7], vcc
	s_cbranch_execz .LBB0_2
	v_mul_f32_e32 v4, 0x3f7d70a4, v3
	v_mul_f32_e32 v4, 0x3fb8aa3b, v4
	v_mul_f32_e32 v3, 0x3c23d70a, v3
	v_exp_f32_e32 v4, v4
	v_mul_f32_e32 v3, 0x3fb8aa3b, v3
	v_exp_f32_e32 v3, v3
	v_lshlrev_b32_e32 v5, 2, v22
	v_or_b32_e32 v6, 0x10a80, v5
	v_mul_f32_e32 v2, 0xbf7d70a4, v2
	ds_write_b32 v6, v4
	v_or_b32_e32 v4, 0x10a00, v5
	v_mul_f32_e32 v2, 0x3fb8aa3b, v2
	ds_write_b32 v4, v3
	v_exp_f32_e32 v4, v2
	v_add_u32_e32 v2, s3, v22
	v_ashrrev_i32_e32 v3, 31, v2
	s_waitcnt lgkmcnt(0)
	v_lshl_add_u64 v[2:3], v[2:3], 2, s[18:19]
	global_store_dword v[2:3], v4, off
.LBB0_2:
	s_or_b64 exec, exec, s[6:7]
	v_bfe_u32 v16, v0, 6, 1
	v_lshl_or_b32 v2, v16, 4, v19
	s_movk_i32 s6, 0x80
	v_and_or_b32 v3, v0, s6, v18
	v_lshlrev_b32_e32 v6, 2, v2
	v_mad_u32_u24 v12, v2, s8, v3
	v_or_b32_e32 v2, 0x10a00, v6
	s_waitcnt lgkmcnt(0)
	s_barrier
	ds_read2_b32 v[10:11], v12 offset1:68
	ds_read_b128 v[2:5], v2
	v_or_b32_e32 v6, 0x10a20, v6
	ds_read_b128 v[6:9], v6
	v_add_u32_e32 v14, 0x800, v12
	v_cmp_gt_u32_e32 vcc, 32, v0
	s_waitcnt lgkmcnt(1)
	v_pk_mul_f32 v[2:3], v[10:11], v[2:3]
	ds_read2_b32 v[10:11], v12 offset0:136 offset1:204
	ds_read2_b32 v[12:13], v14 offset0:32 offset1:100
	ds_read2_b32 v[14:15], v14 offset0:168 offset1:236
	v_cvt_pk_f16_f32 v2, v2, v3
	s_waitcnt lgkmcnt(2)
	v_pk_mul_f32 v[4:5], v[10:11], v[4:5]
	s_nop 0
	v_cvt_pk_f16_f32 v3, v4, v5
	s_waitcnt lgkmcnt(1)
	v_pk_mul_f32 v[4:5], v[12:13], v[6:7]
	s_waitcnt lgkmcnt(0)
	v_pk_mul_f32 v[6:7], v[14:15], v[8:9]
	v_cvt_pk_f16_f32 v4, v4, v5
	v_cvt_pk_f16_f32 v5, v6, v7
	v_lshlrev_b32_e32 v6, 2, v0
	v_and_b32_e32 v6, 0x200, v6
	v_lshl_add_u32 v6, s2, 1, v6
	v_or_b32_e32 v6, v6, v16
	v_ashrrev_i32_e32 v7, 31, v6
	v_lshlrev_b64 v[6:7], 10, v[6:7]
	v_lshl_add_u64 v[6:7], s[12:13], 0, v[6:7]
	v_lshl_add_u64 v[6:7], v[6:7], 0, v[20:21]
	global_store_dwordx4 v[6:7], v[2:5], off
	s_and_saveexec_b64 s[4:5], vcc
	s_cbranch_execz .LBB0_4
	v_lshlrev_b32_e32 v4, 1, v0
	v_bfe_u32 v2, v0, 3, 1
	v_and_b32_e32 v4, 8, v4
	v_and_b32_e32 v3, 16, v0
	v_and_or_b32 v0, v0, 3, v4
	v_lshlrev_b32_e32 v4, 2, v2
	v_or3_b32 v0, v0, v4, v3
	v_lshlrev_b32_e32 v0, 2, v0
	v_or_b32_e32 v4, 0x10a80, v0
	v_or_b32_e32 v0, 0x10a00, v0
	ds_read_b32 v4, v4
	ds_read_b32 v5, v0
	v_lshl_or_b32 v0, v2, 3, s3
	v_or3_b32 v0, v0, v3, v1
	s_waitcnt lgkmcnt(0)
	v_cvt_f16_f32_e32 v4, v4
	v_cvt_f16_f32_e32 v5, v5
	v_ashrrev_i32_e32 v1, 31, v0
	v_lshlrev_b64 v[0:1], 1, v[0:1]
	v_lshl_add_u64 v[2:3], s[14:15], 0, v[0:1]
	v_lshl_add_u64 v[0:1], s[16:17], 0, v[0:1]
	global_store_short v[2:3], v4, off
	global_store_short v[0:1], v5, off
